# in-loop expert-weight fp8 conversion inside the diff-attention tile loop (LDS-staged full-line stores, store issued after loads); last m tiles of each chunk leave cvt_wg pass 2
# speedup vs baseline: 1.0224x; 1.0069x over previous
.LBB0_634:
	s_or_b64 exec, exec, s[0:1]
	s_not_b32 s0, s9
	s_bfe_u32 s73, s2, 0x20006
	s_lshl_b32 s0, s0, 7
	s_ashr_i32 s10, s5, 3
	s_and_b32 s53, s0, 0x1f80
	s_lshl_b32 s0, s73, 5
	s_or_b32 s9, s0, s53
	s_and_b32 s0, s2, 0x3fffffc0
	s_ashr_i32 s11, s10, 31
	v_or_b32_e32 v1, s9, v180
	s_lshl_b32 s0, s0, 2
	s_lshl_b64 s[54:55], s[10:11], 13
	s_add_i32 s95, s0, 0
	v_or_b32_e32 v1, s54, v1
	v_mov_b64_e32 v[4:5], s[88:89]
	s_movk_i32 s0, 0x6880
	v_mad_u64_u32 v[4:5], s[0:1], v1, s0, v[4:5]
	s_lshr_b32 s13, s2, 8
	v_mad_i32_i24 v5, s55, v227, v5
	s_lshl_b32 s42, s4, 8
	v_lshl_add_u64 v[4:5], v[4:5], 0, s[42:43]
	s_lshl_b32 s0, s13, 7
	s_mov_b32 s1, s43
	s_lshr_b32 s12, s2, 6
	s_add_i32 s95, s95, 0x20800
	s_lshl_b32 s72, s4, 7
	v_lshl_add_u64 v[4:5], v[4:5], 0, s[0:1]
	s_mul_i32 s1, s10, 0xd100000
	s_mul_hi_i32 s14, s10, 0xd100000
	s_add_u32 s4, s88, s1
	s_addc_u32 s5, s89, s14
	s_add_u32 s4, s4, s42
	s_addc_u32 s5, s5, 0
	s_lshl_b32 s15, s12, 3
	s_lshr_b32 s10, s2, 4
	v_or_b32_e32 v6, s15, v193
	s_and_b32 s16, s10, 4
	v_mad_u64_u32 v[6:7], s[10:11], v6, s94, v[200:201]
	v_or_b32_e32 v7, s15, v221
	v_bitop3_b32 v1, s15, v228, v218 bitop3:0xc8
	v_mad_u64_u32 v[8:9], s[10:11], v7, s94, v[202:203]
	v_mov_b32_e32 v7, v3
	v_or3_b32 v2, v219, v1, s16
	s_lshl_b32 s10, s12, 11
	v_lshlrev_b64 v[6:7], 1, v[6:7]
	v_mul_lo_u32 v2, v2, s94
	v_lshl_add_u64 v[12:13], s[4:5], 0, v[6:7]
	s_mov_b64 s[18:19], 0x800
	s_add_i32 s52, s10, 0
	v_or_b32_e32 v2, v2, v223
	v_lshl_add_u64 v[12:13], v[12:13], 0, s[18:19]
	s_mov_b32 m0, s52
	s_mov_b64 s[10:11], 0x1000
	global_load_lds_dwordx4 v[12:13], off
	v_lshlrev_b64 v[12:13], 1, v[2:3]
	v_lshl_add_u64 v[14:15], s[4:5], 0, v[12:13]
	v_mov_b32_e32 v9, v3
	v_lshl_add_u64 v[16:17], v[14:15], 0, s[10:11]
	s_add_i32 m0, s52, 0x4000
	v_lshlrev_b64 v[8:9], 1, v[8:9]
	global_load_lds_dwordx4 v[16:17], off
	v_lshl_add_u64 v[16:17], s[4:5], 0, v[8:9]
	v_lshl_add_u64 v[16:17], v[16:17], 0, s[18:19]
	s_add_i32 m0, s52, 0x400
	s_addk_i32 s53, 0x80
	global_load_lds_dwordx4 v[16:17], off
	s_mov_b64 s[10:11], 0x1080
	s_add_i32 m0, s52, 0x4400
	v_lshl_add_u64 v[14:15], v[14:15], 0, s[10:11]
	s_add_u32 s10, s4, 0x1a2800
	s_addc_u32 s11, s5, 0
	s_add_u32 s4, s4, 0x1a3000
	global_load_lds_dwordx4 v[14:15], off
	s_addc_u32 s5, s5, 0
	v_lshl_add_u64 v[6:7], s[10:11], 0, v[6:7]
	s_add_i32 m0, s52, 0x8000
	v_add_u32_e32 v10, 64, v2
	global_load_lds_dwordx4 v[6:7], off
	v_lshl_add_u64 v[6:7], s[4:5], 0, v[12:13]
	s_add_i32 m0, s52, 0xc000
	v_mov_b32_e32 v11, v3
	global_load_lds_dwordx4 v[6:7], off
	v_lshl_add_u64 v[6:7], s[10:11], 0, v[8:9]
	s_add_i32 m0, s52, 0x8400
	v_lshlrev_b32_e32 v2, 1, v182
	global_load_lds_dwordx4 v[6:7], off
	v_lshl_add_u64 v[6:7], v[10:11], 1, s[4:5]
	s_add_i32 m0, s52, 0xc400
	v_lshl_add_u64 v[4:5], v[4:5], 0, v[2:3]
	global_load_lds_dwordx4 v[6:7], off
	global_load_dwordx4 v[132:135], v[4:5], off
	global_load_dwordx4 v[136:139], v[4:5], off offset:32
	global_load_dwordx4 v[140:143], v[4:5], off offset:64
	global_load_dwordx4 v[144:147], v[4:5], off offset:96
	s_lshr_b32 s76, s53, 6
	s_cmp_eq_u32 s13, 1
	s_cselect_b64 s[56:57], -1, 0
	s_cmpk_lt_u32 s2, 0x100
	v_or_b32_e32 v2, s0, v183
	s_cselect_b64 s[58:59], -1, 0
	v_bitop3_b32 v234, s0, v186, v183 bitop3:0x36
	s_movk_i32 s0, 0x60
	s_sub_i32 s77, 0xb0, s9
	s_or_b32 s2, s1, s42
	v_add3_u32 v1, v219, v1, s16
	v_bitop3_b32 v237, v2, v186, s0 bitop3:0x36
	v_mul_lo_u32 v1, v1, s94
	s_add_u32 s0, s92, s2
	v_bitop3_b32 v235, v2, v186, 32 bitop3:0x36
	v_bitop3_b32 v236, v2, v186, 64 bitop3:0x36
	v_or_b32_e32 v2, v223, v1
	s_addc_u32 s1, s93, s14
	v_lshl_add_u64 v[206:207], v[2:3], 1, s[0:1]
	s_mul_i32 s12, s12, 0x1a200
	s_add_u32 s0, s84, s2
	v_add_u32_e32 v2, s12, v224
	s_addc_u32 s1, s97, s14
	v_lshl_add_u64 v[208:209], v[2:3], 1, s[0:1]
	v_add_u32_e32 v2, s12, v225
	v_mov_b32_e32 v16, v3
	v_mov_b32_e32 v17, v3
	v_lshl_add_u64 v[210:211], v[2:3], 1, s[0:1]
	v_mov_b32_e32 v2, v3
	v_mov_b32_e32 v4, v3
	v_mov_b32_e32 v5, v3
	v_mov_b32_e32 v6, v3
	v_mov_b32_e32 v7, v3
	v_mov_b32_e32 v8, v3
	v_mov_b32_e32 v9, v3
	v_mov_b32_e32 v10, v3
	v_mov_b32_e32 v12, v3
	v_mov_b32_e32 v13, v3
	v_mov_b32_e32 v14, v3
	v_mov_b32_e32 v15, v3
	v_mov_b64_e32 v[66:67], v[16:17]
	v_mov_b64_e32 v[50:51], v[16:17]
	v_mov_b64_e32 v[34:35], v[16:17]
	v_mov_b64_e32 v[64:65], v[14:15]
	v_mov_b64_e32 v[62:63], v[12:13]
	v_mov_b64_e32 v[60:61], v[10:11]
	v_mov_b64_e32 v[58:59], v[8:9]
	v_mov_b64_e32 v[56:57], v[6:7]
	v_mov_b64_e32 v[54:55], v[4:5]
	v_mov_b64_e32 v[52:53], v[2:3]
	v_mov_b64_e32 v[48:49], v[14:15]
	v_mov_b64_e32 v[46:47], v[12:13]
	v_mov_b64_e32 v[44:45], v[10:11]
	v_mov_b64_e32 v[42:43], v[8:9]
	v_mov_b64_e32 v[40:41], v[6:7]
	v_mov_b64_e32 v[38:39], v[4:5]
	v_mov_b64_e32 v[36:37], v[2:3]
	v_mov_b64_e32 v[32:33], v[14:15]
	v_mov_b64_e32 v[30:31], v[12:13]
	v_mov_b64_e32 v[28:29], v[10:11]
	v_mov_b64_e32 v[26:27], v[8:9]
	v_mov_b64_e32 v[24:25], v[6:7]
	v_mov_b64_e32 v[22:23], v[4:5]
	v_mov_b64_e32 v[20:21], v[2:3]
	v_mov_b64_e32 v[18:19], v[16:17]
	s_mov_b32 s68, 2
	v_mov_b32_e32 v69, v68
	v_mov_b32_e32 v70, v68
	v_mov_b32_e32 v71, v68
	v_mov_b32_e32 v72, v68
	v_mov_b32_e32 v73, v68
	v_mov_b32_e32 v74, v68
	v_mov_b32_e32 v75, v68
	v_mov_b32_e32 v76, v68
	v_mov_b32_e32 v77, v68
	v_mov_b32_e32 v78, v68
	v_mov_b32_e32 v79, v68
	v_mov_b32_e32 v80, v68
	v_mov_b32_e32 v81, v68
	v_mov_b32_e32 v82, v68
	v_mov_b32_e32 v83, v68
	v_lshl_add_u32 v232, v180, 2, s95
	v_add_u32_e32 v238, s9, v226
	s_mov_b32 s42, 0
	v_mov_b32_e32 v233, 0
	s_mov_b32 s4, 0x10000
	s_mov_b64 s[60:61], 0
	v_mov_b32_e32 v84, 0
	v_mov_b32_e32 v85, 0
	v_mov_b32_e32 v86, 0
	v_mov_b32_e32 v87, 0
	v_mov_b32_e32 v88, 0
	v_mov_b32_e32 v89, 0
	v_mov_b32_e32 v90, 0
	v_mov_b32_e32 v91, 0
	v_mov_b32_e32 v92, 0
	v_mov_b32_e32 v93, 0
	v_mov_b32_e32 v94, 0
	v_mov_b32_e32 v95, 0
	v_mov_b32_e32 v96, 0
	v_mov_b32_e32 v97, 0
	v_mov_b32_e32 v98, 0
	v_mov_b32_e32 v99, 0
	v_mov_b64_e32 v[16:17], v[14:15]
	v_mov_b64_e32 v[14:15], v[12:13]
	v_mov_b64_e32 v[12:13], v[10:11]
	v_mov_b64_e32 v[10:11], v[8:9]
	v_mov_b64_e32 v[8:9], v[6:7]
	v_mov_b64_e32 v[6:7], v[4:5]
	v_mov_b64_e32 v[4:5], v[2:3]
	s_waitcnt vmcnt(0)
	s_add_i32 s0, s76, -1
	s_lshr_b32 s0, s0, 2
	s_sub_i32 s1, 24, s69
	s_min_u32 s0, s0, s1
	s_sub_i32 s5, s1, s0
	s_add_i32 s10, s5, -1
	s_cmp_lt_u32 s10, 3
	s_cbranch_scc0 .Lcvx_mp
	s_add_i32 s0, s1, -4
.Lcvx_mp:
	v_and_b32_e32 v250, 15, v251
	v_lshlrev_b32_e32 v250, 3, v250
	v_mad_u32_u24 v250, v192, 34, v250
	s_lshl_b32 s32, s0, 2
	s_mov_b32 s87, 2
	s_cmp_eq_u32 s0, 0
	s_cbranch_scc1 .Lcvx_pend
	s_mov_b32 s87, 0
	s_andn2_b32 s0, s87, 3
	s_sub_i32 s0, s32, s0
	s_lshr_b32 s0, s0, 2
	s_sub_i32 s0, 24, s0
	s_add_i32 s0, s0, s8
	s_cmpk_gt_i32 s0, 0x3fff
	s_cselect_b32 s16, 13, 14
	s_lshl_b32 s16, 1, s16
	s_and_b32 s1, s87, 3
	s_cmp_lg_u32 s1, 0
	s_cbranch_scc1 .Lcvx_advp
	s_cmpk_gt_i32 s0, 0x3fff
	s_cbranch_scc1 .Lcvx_w2p
	s_lshr_b32 s1, s0, 5
	s_lshl_b32 s1, s1, 21
	s_and_b32 s10, s0, 31
	s_lshl_b32 s11, s10, 9
	s_or_b32 s1, s1, s11
	v_readlane_b32 s12, v254, 39
	v_readlane_b32 s13, v254, 40
	s_branch .Lcvx_tjp
.Lcvx_w2p:
	s_add_i32 s0, s0, 0xffffc000
	s_lshr_b32 s1, s0, 4
	s_lshl_b32 s1, s1, 20
	s_and_b32 s10, s0, 15
	s_lshl_b32 s11, s10, 9
	s_or_b32 s1, s1, s11
	v_readlane_b32 s12, v254, 43
	v_readlane_b32 s13, v254, 44
.Lcvx_tjp:
	s_add_u32 s100, s12, s1
	s_addc_u32 s101, s13, 0
	v_and_b32_e32 v100, 15, v251
	v_mul_u32_u24_e32 v241, s16, v192
	v_lshl_add_u32 v241, v100, 3, v241
	s_branch .Lcvx_ldp
.Lcvx_advp:
	s_add_u32 s100, s100, 0x80
	s_addc_u32 s101, s101, 0
.Lcvx_ldp:
	v_add_u32_e32 v100, s16, v241
	v_add_u32_e32 v101, s16, v100
	v_add_u32_e32 v102, s16, v101
	global_load_dwordx2 v[242:243], v241, s[100:101] nt
	global_load_dwordx2 v[244:245], v100, s[100:101] nt
	global_load_dwordx2 v[246:247], v101, s[100:101] nt
	global_load_dwordx2 v[248:249], v102, s[100:101] nt
	s_mov_b32 s87, 1
.Lcvx_pend:
	s_branch .LBB0_636
.LBB0_635:
	s_add_i32 s4, s4, 0x8000
	s_add_u32 s60, s60, 0x1a2000
	s_addc_u32 s61, s61, 0
	s_add_i32 s68, s68, 1
	s_sub_i32 s42, s42, 64
	s_mul_i32 s0, s76, 0x1a2000
	s_cmp_eq_u32 s0, s60
	v_add_f32_e32 v233, v2, v233
	s_cbranch_scc1 .LBB0_721
.LBB0_636:
	s_add_i32 s0, s87, -2
	s_cmp_lt_u32 s0, s32
	s_cbranch_scc1 .LBB0_640
	s_add_i32 s0, s68, -1
	s_cmp_ge_u32 s0, s76
	s_mov_b64 s[0:1], -1
	s_cbranch_scc0 .LBB0_638
	s_waitcnt vmcnt(0)
	s_mov_b64 s[0:1], 0

.LBB0_640:
	s_cmp_lg_u32 s42, 0
	s_waitcnt lgkmcnt(0)
	s_barrier
	s_cselect_b64 s[62:63], -1, 0
	s_and_b64 s[0:1], s[56:57], s[62:63]
	s_andn2_b64 vcc, exec, s[0:1]
	s_cbranch_vccnz .LBB0_642
	s_add_i32 s0, s4, 0x8000
	s_and_b32 s0, s0, 0x18000
	v_add_u32_e32 v1, s0, v222
	ds_read_b64_tr_b16 v[100:101], v1 offset:0
	ds_read_b64_tr_b16 v[102:103], v1 offset:0x800
	ds_read_b64_tr_b16 v[104:105], v1 offset:0x1000
	ds_read_b64_tr_b16 v[106:107], v1 offset:0x1800
	ds_read_b64_tr_b16 v[108:109], v1 offset:0x2000
	ds_read_b64_tr_b16 v[110:111], v1 offset:0x2800
	ds_read_b64_tr_b16 v[112:113], v1 offset:0x3000
	ds_read_b64_tr_b16 v[114:115], v1 offset:0x3800
	ds_read_b64_tr_b16 v[116:117], v1 offset:0x200
	ds_read_b64_tr_b16 v[118:119], v1 offset:0xa00
	ds_read_b64_tr_b16 v[120:121], v1 offset:0x1200
	ds_read_b64_tr_b16 v[122:123], v1 offset:0x1a00
	ds_read_b64_tr_b16 v[124:125], v1 offset:0x2200
	ds_read_b64_tr_b16 v[126:127], v1 offset:0x2a00
	ds_read_b64_tr_b16 v[128:129], v1 offset:0x3200
	ds_read_b64_tr_b16 v[130:131], v1 offset:0x3a00
	s_waitcnt lgkmcnt(8)
	s_nop 0
	v_mfma_f32_32x32x16_bf16 v[52:67], v[96:99], v[100:103], v[52:67]
	v_mfma_f32_32x32x16_bf16 v[52:67], v[92:95], v[104:107], v[52:67]
	v_mfma_f32_32x32x16_bf16 v[52:67], v[88:91], v[108:111], v[52:67]
	v_mfma_f32_32x32x16_bf16 v[52:67], v[84:87], v[112:115], v[52:67]
	ds_read_b64_tr_b16 v[100:101], v1 offset:0x400
	ds_read_b64_tr_b16 v[102:103], v1 offset:0xc00
	ds_read_b64_tr_b16 v[104:105], v1 offset:0x1400
	ds_read_b64_tr_b16 v[106:107], v1 offset:0x1c00
	ds_read_b64_tr_b16 v[108:109], v1 offset:0x2400
	ds_read_b64_tr_b16 v[110:111], v1 offset:0x2c00
	ds_read_b64_tr_b16 v[112:113], v1 offset:0x3400
	ds_read_b64_tr_b16 v[114:115], v1 offset:0x3c00
	s_waitcnt lgkmcnt(8)
	v_mfma_f32_32x32x16_bf16 v[36:51], v[96:99], v[116:119], v[36:51]
	v_mfma_f32_32x32x16_bf16 v[36:51], v[92:95], v[120:123], v[36:51]
	v_mfma_f32_32x32x16_bf16 v[36:51], v[88:91], v[124:127], v[36:51]
	v_mfma_f32_32x32x16_bf16 v[36:51], v[84:87], v[128:131], v[36:51]
	ds_read_b64_tr_b16 v[116:117], v1 offset:0x600
	ds_read_b64_tr_b16 v[118:119], v1 offset:0xe00
	ds_read_b64_tr_b16 v[120:121], v1 offset:0x1600
	ds_read_b64_tr_b16 v[122:123], v1 offset:0x1e00
	ds_read_b64_tr_b16 v[124:125], v1 offset:0x2600
	ds_read_b64_tr_b16 v[126:127], v1 offset:0x2e00
	ds_read_b64_tr_b16 v[128:129], v1 offset:0x3600
	ds_read_b64_tr_b16 v[130:131], v1 offset:0x3e00
	s_waitcnt lgkmcnt(8)
	v_mfma_f32_32x32x16_bf16 v[20:35], v[96:99], v[100:103], v[20:35]
	v_mfma_f32_32x32x16_bf16 v[20:35], v[92:95], v[104:107], v[20:35]
	v_mfma_f32_32x32x16_bf16 v[20:35], v[88:91], v[108:111], v[20:35]
	v_mfma_f32_32x32x16_bf16 v[20:35], v[84:87], v[112:115], v[20:35]
	s_waitcnt lgkmcnt(0)
	v_mfma_f32_32x32x16_bf16 v[4:19], v[96:99], v[116:119], v[4:19]
	v_mfma_f32_32x32x16_bf16 v[4:19], v[92:95], v[120:123], v[4:19]
	v_mfma_f32_32x32x16_bf16 v[4:19], v[88:91], v[124:127], v[4:19]
	v_mfma_f32_32x32x16_bf16 v[4:19], v[84:87], v[128:131], v[4:19]

.LBB0_719:
	s_add_i32 s17, s87, -2
	s_cmp_lt_u32 s17, s32
	s_cselect_b64 s[18:19], -1, 0
	s_cbranch_scc0 .Lcvx_c1x
	s_and_b32 s1, s17, 1
	s_mulk_i32 s1, 0x1100
	s_add_i32 s1, s1, 0x21800
	v_add_u32_e32 v95, s1, v250
	ds_read_b64 v[252:253], v95
.Lcvx_c1x:
	s_add_i32 s0, s87, -1
	s_cmp_lt_u32 s0, s32
	s_cbranch_scc0 .Lcvx_ncv
	s_and_b32 s1, s0, 1
	s_mulk_i32 s1, 0x1100
	s_add_i32 s1, s1, 0x21800
	s_movk_i32 s10, 0x110
	v_and_b32_e32 v92, 15, v251
	v_mad_u32_u24 v92, v92, s10, v192
	v_add_u32_e32 v92, s1, v92
	s_add_i32 s1, s87, -3
	s_cmp_lt_u32 s1, s32
	s_cbranch_scc1 .Lcvx_ws
	s_cmp_ge_u32 s68, s76
	s_cbranch_scc1 .Lcvx_w0
	s_waitcnt vmcnt(4)
	s_branch .Lcvx_cv
.Lcvx_w0:
	s_waitcnt vmcnt(0)
	s_branch .Lcvx_cv
.Lcvx_ws:
	s_cmp_ge_u32 s68, s76
	s_cbranch_scc1 .Lcvx_w1
	s_waitcnt vmcnt(5)
	s_branch .Lcvx_cv
.Lcvx_w1:
	s_waitcnt vmcnt(1)
.Lcvx_cv:
	v_pk_mul_f32 v[242:243], v[242:243], s[98:99]
	v_pk_mul_f32 v[244:245], v[244:245], s[98:99]
	v_pk_mul_f32 v[246:247], v[246:247], s[98:99]
	v_pk_mul_f32 v[248:249], v[248:249], s[98:99]
	v_cvt_pk_fp8_f32 v242, v242, v244
	v_cvt_pk_fp8_f32 v243, v243, v245
	v_cvt_pk_fp8_f32 v242, v246, v248 op_sel:[0,0,1]
	v_cvt_pk_fp8_f32 v243, v247, v249 op_sel:[0,0,1]
	s_nop 0
	ds_write2_b32 v92, v242, v243 offset1:34
.Lcvx_ncv:
	s_cmp_lt_u32 s87, s32
	s_cbranch_scc0 .Lcvx_nis
	s_andn2_b32 s0, s87, 3
	s_sub_i32 s0, s32, s0
	s_lshr_b32 s0, s0, 2
	s_sub_i32 s0, 24, s0
	s_add_i32 s0, s0, s8
	s_cmpk_gt_i32 s0, 0x3fff
	s_cselect_b32 s16, 13, 14
	s_lshl_b32 s16, 1, s16
	s_and_b32 s1, s87, 3
	s_cmp_lg_u32 s1, 0
	s_cbranch_scc1 .Lcvx_advb
	s_cmpk_gt_i32 s0, 0x3fff
	s_cbranch_scc1 .Lcvx_w2b
	s_lshr_b32 s1, s0, 5
	s_lshl_b32 s1, s1, 21
	s_and_b32 s10, s0, 31
	s_lshl_b32 s11, s10, 9
	s_or_b32 s1, s1, s11
	v_readlane_b32 s12, v254, 39
	v_readlane_b32 s13, v254, 40
	s_branch .Lcvx_tjb

.Lcvx_tjb:
	s_add_u32 s100, s12, s1
	s_addc_u32 s101, s13, 0
	v_and_b32_e32 v92, 15, v251
	v_mul_u32_u24_e32 v241, s16, v192
	v_lshl_add_u32 v241, v92, 3, v241
	s_branch .Lcvx_ldb

.Lcvx_ldb:
	v_add_u32_e32 v92, s16, v241
	v_add_u32_e32 v93, s16, v92
	v_add_u32_e32 v94, s16, v93
	global_load_dwordx2 v[242:243], v241, s[100:101] nt
	global_load_dwordx2 v[244:245], v92, s[100:101] nt
	global_load_dwordx2 v[246:247], v93, s[100:101] nt
	global_load_dwordx2 v[248:249], v94, s[100:101] nt
.Lcvx_nis:
	s_andn2_b64 vcc, exec, s[18:19]
	s_cbranch_vccnz .Lcvx_nst
	s_andn2_b32 s1, s17, 3
	s_sub_i32 s1, s32, s1
	s_lshr_b32 s1, s1, 2
	s_sub_i32 s1, 24, s1
	s_add_i32 s1, s1, s8
	s_and_b32 s5, s17, 3
	s_cmpk_gt_i32 s1, 0x3fff
	s_cbranch_scc1 .Lcvx_ow2
	s_and_b32 s10, s1, 31
	s_lshr_b32 s11, s1, 9
	s_lshl_b32 s11, s11, 12
	s_and_b32 s14, s10, 15
	s_lshl_b32 s14, s14, 8
	s_or_b32 s11, s11, s14
	s_lshr_b32 s14, s10, 4
	s_lshl_b32 s14, s14, 7
	s_or_b32 s11, s11, s14
	s_bfe_u32 s14, s1, 0x40005
	s_mov_b32 s15, 0x5600000
	s_branch .Lcvx_oj
.Lcvx_ow2:
	s_add_i32 s1, s1, 0xffffc000
	s_and_b32 s10, s1, 15
	s_lshr_b32 s11, s1, 8
	s_lshl_b32 s11, s11, 11
	s_lshl_b32 s14, s10, 7
	s_or_b32 s11, s11, s14
	s_bfe_u32 s14, s1, 0x40004
	s_mov_b32 s15, 0x16700000
.Lcvx_oj:
	s_lshl_b32 s5, s5, 5
	s_add_i32 s11, s11, s5
	s_mul_i32 s11, s11, 0x880
	s_add_i32 s11, s11, s15
	s_lshl_b32 s14, s14, 7
	s_add_i32 s11, s11, s14
	s_movk_i32 s10, 0x1fe
	v_mad_u32_u24 v95, v192, s10, v250
	v_add_u32_e32 v95, s11, v95
	s_waitcnt lgkmcnt(0)
	global_store_dwordx2 v95, v[252:253], s[92:93] nt
.Lcvx_nst:
	s_add_i32 s0, s32, 2
	s_add_i32 s87, s87, 1
	s_min_u32 s87, s87, s0
	v_cvt_pk_bf16_f32 v96, v123, v127
	v_cvt_pk_bf16_f32 v97, v124, v126
	v_cvt_pk_bf16_f32 v98, v125, v129
	v_cvt_pk_bf16_f32 v99, v122, v128
	v_cvt_pk_bf16_f32 v92, v89, v91
	v_cvt_pk_bf16_f32 v93, v88, v90
	v_cvt_pk_bf16_f32 v94, v107, v109
	v_cvt_pk_bf16_f32 v95, v106, v108
	v_cvt_pk_bf16_f32 v88, v117, v119
	v_cvt_pk_bf16_f32 v89, v84, v118
	v_cvt_pk_bf16_f32 v90, v85, v121
	v_cvt_pk_bf16_f32 v91, v116, v120
	v_cvt_pk_bf16_f32 v84, v87, v101
	v_cvt_pk_bf16_f32 v85, v86, v100
	v_cvt_pk_bf16_f32 v86, v103, v105
	v_cvt_pk_bf16_f32 v87, v102, v104
	s_nop 0
	v_permlane32_swap_b32_e32 v96, v98
	v_permlane32_swap_b32_e32 v97, v99
	v_permlane32_swap_b32_e32 v92, v94
	v_permlane32_swap_b32_e32 v93, v95
	v_permlane32_swap_b32_e32 v88, v90
	v_permlane32_swap_b32_e32 v89, v91
	v_permlane32_swap_b32_e32 v84, v86
	v_permlane32_swap_b32_e32 v85, v87
	v_cndmask_b32_e64 v1, 0, 1, s[58:59]
	v_cmp_ne_u32_e64 s[10:11], 1, v1
	s_andn2_b64 vcc, exec, s[58:59]
	s_cbranch_vccnz .LBB0_635
	v_add_u32_e32 v1, s2, v222
	ds_read_b64_tr_b16 v[100:101], v1 offset:0
	ds_read_b64_tr_b16 v[102:103], v1 offset:0x800
	ds_read_b64_tr_b16 v[104:105], v1 offset:0x1000
	ds_read_b64_tr_b16 v[106:107], v1 offset:0x1800
	ds_read_b64_tr_b16 v[108:109], v1 offset:0x2000
	ds_read_b64_tr_b16 v[110:111], v1 offset:0x2800
	ds_read_b64_tr_b16 v[112:113], v1 offset:0x3000
	ds_read_b64_tr_b16 v[114:115], v1 offset:0x3800
	ds_read_b64_tr_b16 v[116:117], v1 offset:0x200
	ds_read_b64_tr_b16 v[118:119], v1 offset:0xa00
	ds_read_b64_tr_b16 v[120:121], v1 offset:0x1200
	ds_read_b64_tr_b16 v[122:123], v1 offset:0x1a00
	ds_read_b64_tr_b16 v[124:125], v1 offset:0x2200
	ds_read_b64_tr_b16 v[126:127], v1 offset:0x2a00
	ds_read_b64_tr_b16 v[128:129], v1 offset:0x3200
	ds_read_b64_tr_b16 v[130:131], v1 offset:0x3a00
	s_waitcnt lgkmcnt(8)
	s_nop 0
	v_mfma_f32_32x32x16_bf16 v[52:67], v[96:99], v[100:103], v[52:67]
	v_mfma_f32_32x32x16_bf16 v[52:67], v[92:95], v[104:107], v[52:67]
	v_mfma_f32_32x32x16_bf16 v[52:67], v[88:91], v[108:111], v[52:67]
	v_mfma_f32_32x32x16_bf16 v[52:67], v[84:87], v[112:115], v[52:67]
	ds_read_b64_tr_b16 v[100:101], v1 offset:0x400
	ds_read_b64_tr_b16 v[102:103], v1 offset:0xc00
	ds_read_b64_tr_b16 v[104:105], v1 offset:0x1400
	ds_read_b64_tr_b16 v[106:107], v1 offset:0x1c00
	ds_read_b64_tr_b16 v[108:109], v1 offset:0x2400
	ds_read_b64_tr_b16 v[110:111], v1 offset:0x2c00
	ds_read_b64_tr_b16 v[112:113], v1 offset:0x3400
	ds_read_b64_tr_b16 v[114:115], v1 offset:0x3c00
	s_waitcnt lgkmcnt(8)
	v_mfma_f32_32x32x16_bf16 v[36:51], v[96:99], v[116:119], v[36:51]
	v_mfma_f32_32x32x16_bf16 v[36:51], v[92:95], v[120:123], v[36:51]
	v_mfma_f32_32x32x16_bf16 v[36:51], v[88:91], v[124:127], v[36:51]
	v_mfma_f32_32x32x16_bf16 v[36:51], v[84:87], v[128:131], v[36:51]
	ds_read_b64_tr_b16 v[116:117], v1 offset:0x600
	ds_read_b64_tr_b16 v[118:119], v1 offset:0xe00
	ds_read_b64_tr_b16 v[120:121], v1 offset:0x1600
	ds_read_b64_tr_b16 v[122:123], v1 offset:0x1e00
	ds_read_b64_tr_b16 v[124:125], v1 offset:0x2600
	ds_read_b64_tr_b16 v[126:127], v1 offset:0x2e00
	ds_read_b64_tr_b16 v[128:129], v1 offset:0x3600
	ds_read_b64_tr_b16 v[130:131], v1 offset:0x3e00
	s_waitcnt lgkmcnt(8)
	v_mfma_f32_32x32x16_bf16 v[20:35], v[96:99], v[100:103], v[20:35]
	v_mfma_f32_32x32x16_bf16 v[20:35], v[92:95], v[104:107], v[20:35]
	v_mfma_f32_32x32x16_bf16 v[20:35], v[88:91], v[108:111], v[20:35]
	v_mfma_f32_32x32x16_bf16 v[20:35], v[84:87], v[112:115], v[20:35]
	s_waitcnt lgkmcnt(0)
	v_mfma_f32_32x32x16_bf16 v[4:19], v[96:99], v[116:119], v[4:19]
	v_mfma_f32_32x32x16_bf16 v[4:19], v[92:95], v[120:123], v[4:19]
	v_mfma_f32_32x32x16_bf16 v[4:19], v[88:91], v[124:127], v[4:19]
	v_mfma_f32_32x32x16_bf16 v[4:19], v[84:87], v[128:131], v[4:19]
	s_branch .LBB0_635

.LBB0_729:
	s_add_i32 s0, s76, -1
	s_lshr_b32 s0, s0, 2
	s_sub_i32 s1, 24, s69
	s_min_u32 s0, s0, s1
	s_sub_i32 s5, s1, s0
	s_add_i32 s10, s5, -1
	s_cmp_lt_u32 s10, 3
	s_cbranch_scc0 .Lcvx_me
	s_add_i32 s0, s1, -4
.Lcvx_me:
	s_sub_i32 s71, s1, s0
	s_cmp_eq_u32 s71, 0
	s_cbranch_scc1 .LBB0_553
	s_add_i32 s8, s8, s69
	s_cmpk_gt_i32 s8, 0x3fff
	s_mov_b64 s[10:11], -1
	s_waitcnt vmcnt(63) expcnt(7) lgkmcnt(15)
	s_barrier
	s_cbranch_scc0 .LBB0_731
	s_add_i32 s0, s8, 0xffffc000
	s_lshr_b32 s42, s0, 8
	s_lshl_b32 s0, s8, 3
	s_and_b32 s12, s0, 0x780
	s_lshl_b32 s0, s8, 7
	v_readlane_b32 s16, v254, 31
	s_and_b32 s2, s0, 0x700
	s_lshl_b64 s[14:15], s[42:43], 11
	s_lshl_b64 s[0:1], s[42:43], 24
	v_readlane_b32 s28, v254, 43
	v_readlane_b32 s29, v254, 44
	s_add_u32 s0, s28, s0
	s_addc_u32 s1, s29, s1
	s_lshl_b32 s4, s12, 13
	s_add_u32 s0, s0, s4
	s_addc_u32 s1, s1, 0
	s_lshl_b32 s4, s2, 2
	s_add_u32 s0, s0, s4
	v_readlane_b32 s17, v254, 32
	v_readlane_b32 s18, v254, 33
	v_readlane_b32 s19, v254, 34
	v_readlane_b32 s20, v254, 35
	v_readlane_b32 s21, v254, 36
	v_readlane_b32 s22, v254, 37
	v_readlane_b32 s23, v254, 38
	v_readlane_b32 s24, v254, 39
	v_readlane_b32 s25, v254, 40
	v_readlane_b32 s26, v254, 41
	v_readlane_b32 s27, v254, 42
	v_readlane_b32 s30, v254, 45
	v_readlane_b32 s31, v254, 46
	s_mov_b32 s13, s43
	s_addc_u32 s1, s1, 0
	s_or_b32 s14, s14, s2
	s_mov_b64 s[10:11], 0
